# M1: the four token-index (gather list) loads of each unit are issued together with one wait instead of four dependent load->wait pairs (per unit and at phase start)
# speedup vs baseline: 1.0169x; 1.0169x over previous
; #define PG8_STAGE_B(bufoff, gbase) PG8_STAGE_U(bufoff, gbase, voffB, qstepB)
; #define PG8_STAGE_A(bufoff, gbase, h, GO) do { if constexpr (GATHER) { PG8_STAGE(bufoff, gbase, (GO)[h]); } else { PG8_STAGE_U(bufoff, (const char*)(gbase) + (h) * hstepA, voffA, qstepA); } } while (0)
; #define PG8_WAIT_V(n) asm volatile("s_waitcnt vmcnt(" #n ")" ::: "memory")
; #define PG8_BAR __builtin_amdgcn_s_barrier()
; #define PG8_GOFF(dst, U) do { _Pragma("unroll") for (int _h = 0; _h < 2; ++_h) _Pragma("unroll") for (int _i = 0; _i < 2; ++_i) { int _R, _C; stage_rc(tid * 16 + _i * 8192, _R, _C); dst[_h][_i] = (unsigned)S.gather_row(U, _h * HALF + _R); } } while (0)
; #define PG8_GCVT(dst) do { _Pragma("unroll") for (int _h = 0; _h < 2; ++_h) _Pragma("unroll") for (int _i = 0; _i < 2; ++_i) { int _R, _C; stage_rc(tid * 16 + _i * 8192, _R, _C); dst[_h][_i] = dst[_h][_i] * (unsigned)(lda * 2) + (unsigned)(_C * 2); } } while (0)
;     ...
; #pragma unroll
;     for (int h = 0; h < 2; ++h)
; #pragma unroll
;         for (int i = 0; i < 2; ++i) { gc[h][i] = 0; gn[h][i] = 0; }
;     if constexpr (GATHER) { PG8_GOFF(gc, cur); PG8_GCVT(gc); }
;     PG8_STAGE_B(PG8_SB(0, 0), cB); PG8_STAGE_B(PG8_SB(0, 1), cB + hstepB); PG8_STAGE_A(PG8_SA(0, 0), cA, 0, gc); PG8_STAGE_A(PG8_SA(0, 1), cA, 1, gc);
;     if (wr == 1) PG8_BAR;
;     PG8_WAIT_V(2); PG8_BAR;
;     PG8_STAGE_B(PG8_SB(1, 0), cB + kstep); PG8_STAGE_A(PG8_SA(1, 0), cA + kstep, 0, gc); PG8_STAGE_B(PG8_SB(1, 1), cB + hstepB + kstep);
;     PG8_WAIT_V(6); PG8_BAR;
;     DI int gather_row(const Unit& u, int r) const {
;         const int li = u.j * 256 + r; const int n = u.n;
;         const char* lb = (const char*)lists + (size_t)u.e * LIST_CAP * 8;
;         int tok = 0; if (li < n) tok = *(const int*)(lb + (unsigned)li * 8u) >> 2;
;         return tok;
;     }
.LBB0_1188:
	s_andn2_b64 vcc, exec, s[12:13]
	s_cbranch_vccnz .LBB0_1242
	v_bfe_i32 v3, v2, 27, 1
	v_lshlrev_b32_e32 v7, 4, v2
	v_lshrrev_b32_e32 v3, 22, v3
	v_ashrrev_i32_e32 v0, 31, v2
	v_add_u32_e32 v3, v7, v3
	v_lshrrev_b32_e32 v0, 26, v0
	v_and_b32_e32 v3, 0xfffffc00, v3
	v_add_u32_e32 v0, v2, v0
	v_sub_u32_e32 v3, v7, v3
	v_ashrrev_i32_e32 v0, 6, v0
	v_lshrrev_b32_e32 v4, 4, v3
	v_bitop3_b32 v4, v4, v3, 32 bitop3:0x6c
	v_lshlrev_b32_e32 v3, 3, v0
	v_and_b32_e32 v5, -16, v3
	v_ashrrev_i32_e32 v3, 31, v4
	v_lshrrev_b32_e32 v3, 26, v3
	v_add_u32_e32 v3, v4, v3
	s_add_u32 s16, s4, 0x400000
	v_ashrrev_i32_e32 v3, 6, v3
	s_addc_u32 s17, s5, 0
	s_ashr_i32 s3, s2, 31
	v_add_u32_e32 v214, v3, v5
	s_lshl_b64 s[12:13], s[2:3], 18
	s_add_u32 s12, s16, s12
	v_add_u32_e32 v8, s7, v214
	s_mov_b32 s55, s20
	s_mov_b32 s54, s16
	s_mov_b32 s61, s17
	s_addc_u32 s13, s17, s13
	v_cmp_gt_i32_e32 vcc, s18, v8
	v_mov_b32_e32 v5, 0
	v_mov_b32_e32 v6, 0
	s_and_saveexec_b64 s[16:17], vcc
	s_cbranch_execz .LBB0_1191
	v_lshlrev_b32_e32 v6, 3, v8
	global_load_dword v6, v6, s[12:13]
.LBB0_1191:
	s_or_b64 exec, exec, s[16:17]
	v_add_u32_e32 v8, 0x2000, v7
	v_ashrrev_i32_e32 v7, 31, v8
	v_lshrrev_b32_e32 v7, 22, v7
	v_add_u32_e32 v7, v8, v7
	v_ashrrev_i32_e32 v7, 10, v7
	v_mul_i32_i24_e32 v9, 0x400, v7
	v_sub_u32_e32 v8, v8, v9
	v_lshrrev_b32_e32 v9, 4, v8
	v_bitop3_b32 v8, v9, v8, 32 bitop3:0x6c
	v_lshlrev_b32_e32 v9, 3, v7
	v_and_b32_e32 v10, -16, v9
	v_ashrrev_i32_e32 v9, 31, v8
	v_lshrrev_b32_e32 v9, 26, v9
	v_add_u32_e32 v9, v8, v9
	v_ashrrev_i32_e32 v9, 6, v9
	v_add_u32_e32 v215, v9, v10
	v_add_u32_e32 v10, s7, v215
	v_cmp_gt_i32_e32 vcc, s18, v10
	s_and_saveexec_b64 s[16:17], vcc
	v_readlane_b32 s60, v253, 27
	s_mov_b32 s73, s19
	s_cbranch_execz .LBB0_1193
	v_lshlrev_b32_e32 v5, 3, v10
	global_load_dword v5, v5, s[12:13]
.LBB0_1193:
	s_or_b64 exec, exec, s[16:17]
	s_or_b32 s3, s7, 0x80
	v_add_u32_e32 v12, s3, v214
	v_cmp_gt_i32_e32 vcc, s18, v12
	v_mov_b32_e32 v10, 0
	v_mov_b32_e32 v11, 0
	s_and_saveexec_b64 s[16:17], vcc
	s_cbranch_execz .LBB0_1195
	v_lshlrev_b32_e32 v11, 3, v12
	global_load_dword v11, v11, s[12:13]
.LBB0_1195:
	s_mov_b64 s[20:21], s[44:45]
	s_or_b64 exec, exec, s[16:17]
	v_add_u32_e32 v12, s3, v215
	v_cmp_gt_i32_e32 vcc, s18, v12
	s_and_saveexec_b64 s[16:17], vcc
	s_cbranch_execz .LBB0_1197
	v_lshlrev_b32_e32 v10, 3, v12
	global_load_dword v10, v10, s[12:13]
.LBB0_1197:
	v_writelane_b32 v255, s38, 16
	v_writelane_b32 v255, s97, 22
	s_or_b64 exec, exec, s[16:17]
	s_waitcnt vmcnt(0)
	v_lshlrev_b32_e32 v6, 8, v6
	v_and_b32_e32 v6, 0xfffffc00, v6
	v_lshlrev_b32_e32 v5, 8, v5
	v_and_b32_e32 v5, 0xfffffc00, v5
	v_lshlrev_b32_e32 v11, 8, v11
	v_and_b32_e32 v11, 0xfffffc00, v11
	v_lshlrev_b32_e32 v10, 8, v10
	v_and_b32_e32 v10, 0xfffffc00, v10
	v_lshlrev_b32_e32 v12, 6, v3
	v_sub_u32_e32 v4, v4, v12
	v_mov_b32_e32 v14, 1
	v_lshlrev_b32_e32 v0, 5, v0
	v_ashrrev_i16_sdwa v4, v14, sext(v4) dst_sel:DWORD dst_unused:UNUSED_PAD src0_sel:DWORD src1_sel:BYTE_0
	v_lshlrev_b32_e32 v12, 1, v214
	v_lshrrev_b32_e32 v13, 2, v214
	v_and_b32_e32 v3, 3, v3
	s_mov_b32 s7, 0x3fffe0
	v_and_b32_e32 v0, 32, v0
	v_bfe_i32 v4, v4, 0, 16
	v_and_b32_e32 v12, 24, v12
	v_and_b32_e32 v13, 4, v13
	v_and_or_b32 v3, v214, s7, v3
	v_or3_b32 v3, v3, v13, v12
	v_add_lshl_u32 v216, v0, v4, 1
	v_lshl_add_u32 v217, v3, 10, v216
	v_lshlrev_b32_e32 v3, 6, v9
	s_ashr_i32 s3, s1, 6
	v_sub_u32_e32 v3, v8, v3
	s_lshl_b32 s7, s3, 10
	v_lshlrev_b32_e32 v0, 5, v7
	v_ashrrev_i16_sdwa v3, v14, sext(v3) dst_sel:DWORD dst_unused:UNUSED_PAD src0_sel:DWORD src1_sel:BYTE_0
	v_and_b32_e32 v0, 32, v0
	v_bfe_i32 v3, v3, 0, 16
	s_add_i32 s63, s7, 0
	v_add_lshl_u32 v219, v0, v3, 1
	s_add_i32 s78, s63, 0x10000
	v_mov_b32_e32 v0, v217
	s_mov_b32 m0, s78
	v_add_u32_e32 v222, v5, v219
	global_load_lds_dwordx4 v0, s[8:9]
	v_mov_b32_e32 v0, v217
	s_add_i32 s79, s63, 0x12000
	v_lshl_add_u64 v[4:5], s[8:9], 0, v[0:1]
	v_lshl_add_u64 v[4:5], v[4:5], 0, s[74:75]
	s_mov_b32 m0, s79
	v_mov_b32_e32 v0, v217
	global_load_lds_dwordx4 v[4:5], off
	s_add_i32 s95, s63, 0x14000
	s_mov_b32 m0, s95
	v_lshl_add_u64 v[4:5], s[8:9], 0, v[0:1]
	v_lshl_add_u64 v[4:5], v[4:5], 0, s[80:81]
	v_mov_b32_e32 v0, v217
	v_add_u32_e32 v218, v6, v216
	global_load_lds_dwordx4 v[4:5], off
	s_add_i32 s39, s63, 0x16000
	v_lshl_add_u64 v[4:5], s[8:9], 0, v[0:1]
	v_lshl_add_u64 v[4:5], v[4:5], 0, s[82:83]
	s_mov_b32 m0, s39
	v_mov_b32_e32 v0, v218
	global_load_lds_dwordx4 v[4:5], off
	s_mov_b32 m0, s63
	s_add_i32 s33, s63, 0x2000
	global_load_lds_dwordx4 v0, s[10:11]
	v_mov_b32_e32 v0, v222
	v_add_u32_e32 v221, v11, v216
	s_mov_b32 m0, s33
	s_add_i32 s76, s63, 0x4000
	global_load_lds_dwordx4 v0, s[10:11]
	v_mov_b32_e32 v0, v221
	v_add_u32_e32 v220, v10, v219
	s_mov_b32 m0, s76
	s_add_i32 s77, s63, 0x6000
	global_load_lds_dwordx4 v0, s[10:11]
	v_mov_b32_e32 v0, v220
	s_mov_b32 m0, s77
	s_ashr_i32 s7, s1, 8
	global_load_lds_dwordx4 v0, s[10:11]
	s_cmp_eq_u32 s7, 1
	s_cselect_b64 s[12:13], -1, 0
	v_writelane_b32 v255, s12, 18
	s_cmp_lg_u32 s7, 1
	s_nop 0
	v_writelane_b32 v255, s13, 19
	s_cbranch_scc1 .LBB0_1199
	s_barrier

; #define PG8_GOFF(dst, U) do { _Pragma("unroll") for (int _h = 0; _h < 2; ++_h) _Pragma("unroll") for (int _i = 0; _i < 2; ++_i) { int _R, _C; stage_rc(tid * 16 + _i * 8192, _R, _C); dst[_h][_i] = (unsigned)S.gather_row(U, _h * HALF + _R); } } while (0)
;     ...
;         if constexpr (GATHER) { if (has_next) PG8_GOFF(gn, nxt); }
;     DI int gather_row(const Unit& u, int r) const {
;         const int li = u.j * 256 + r; const int n = u.n;
;         const char* lb = (const char*)lists + (size_t)u.e * LIST_CAP * 8;
;         int tok = 0; if (li < n) tok = *(const int*)(lb + (unsigned)li * 8u) >> 2;
;         return tok;
;     }
.LBB0_1205:
	v_cndmask_b32_e64 v0, 0, 1, s[26:27]
	v_cmp_ne_u32_e64 s[4:5], 1, v0
	s_andn2_b64 vcc, exec, s[26:27]
	s_cbranch_vccnz .LBB0_1215
	s_ashr_i32 s17, s16, 31
	s_lshl_b32 s1, s57, 8
	s_lshl_b64 s[22:23], s[16:17], 18
	s_add_u32 s22, s54, s22
	s_addc_u32 s23, s61, s23
	v_mov_b32_e32 v225, 0
	v_mov_b32_e32 v226, 0
	v_mov_b32_e32 v227, 0
	v_mov_b32_e32 v228, 0
	v_add_u32_e32 v0, s1, v214
	v_cmp_gt_i32_e32 vcc, s13, v0
	s_and_saveexec_b64 s[28:29], vcc
	v_lshlrev_b32_e32 v0, 3, v0
	global_load_dword v226, v0, s[22:23]
	s_or_b64 exec, exec, s[28:29]
	v_add_u32_e32 v0, s1, v215
	v_cmp_gt_i32_e32 vcc, s13, v0
	s_and_saveexec_b64 s[28:29], vcc
	v_lshlrev_b32_e32 v0, 3, v0
	global_load_dword v225, v0, s[22:23]
	s_or_b64 exec, exec, s[28:29]
	s_bitset1_b32 s1, 7
	v_add_u32_e32 v0, s1, v214
	v_cmp_gt_i32_e32 vcc, s13, v0
	s_and_saveexec_b64 s[28:29], vcc
	v_lshlrev_b32_e32 v0, 3, v0
	global_load_dword v228, v0, s[22:23]
	s_or_b64 exec, exec, s[28:29]
	v_add_u32_e32 v0, s1, v215
	v_cmp_gt_i32_e32 vcc, s13, v0
	s_and_saveexec_b64 s[28:29], vcc
	v_lshlrev_b32_e32 v0, 3, v0
	global_load_dword v227, v0, s[22:23]
	s_or_b64 exec, exec, s[28:29]
	s_waitcnt vmcnt(0)
	v_ashrrev_i32_e32 v226, 2, v226
	v_ashrrev_i32_e32 v225, 2, v225
	v_ashrrev_i32_e32 v228, 2, v228
	v_ashrrev_i32_e32 v227, 2, v227
